# v103 + GEMM4 K-loop: LDS-DMA loads issued at the top of each load segment (before the ds_reads), 4 per segment, SGPR-base DMA form
# baseline (speedup 1.0000x reference)
; #define PG8_STAGE(bufoff, gbase, voff) do { _Pragma("unroll") for (int _i = 0; _i < 2; ++_i) \
;         __builtin_amdgcn_global_load_lds((const unsigned*)((const char*)(gbase) + (voff)[_i]), (PG8_LAS unsigned*)(lds + (bufoff) + ldsw + _i * 8192), 16, 0, 0); } while (0)
; #define PG8_WAIT_V(n) asm volatile("s_waitcnt vmcnt(" #n ")" ::: "memory")
; #define PG8_BAR __builtin_amdgcn_s_barrier()
; template <class Epi, class Sched, bool ALIGN_EPI = false, bool SP2 = false, bool F8 = false>
; __device__ __forceinline__ void gemm_phase(PG8_LAS unsigned char* lds, const Gemm g_in, const Sched& S, const Epi& E, int wave_in) {
;     ...
;     const int aoff = lds_byte(wr * 64 + fr, fq * 8), boff = lds_byte(wc * 32 + fr, fq * 8);
;     ...
;         PG8_STAGE(PG8_SB(0, 0), cB, voffB); PG8_STAGE(PG8_SB(0, 1), cB + hstepB, voffB); PG8_STAGE(PG8_SA(0, 0), cA, voffA); PG8_STAGE(PG8_SA(0, 1), cA + hstepA, voffA);
;         if (wr == 1) PG8_BAR;
;         PG8_WAIT_V(2); PG8_BAR;
;         PG8_STAGE(PG8_SB(1, 0), cB + kstep, voffB); PG8_STAGE(PG8_SA(1, 0), cA + kstep, voffA); PG8_STAGE(PG8_SB(1, 1), cB + hstepB + kstep, voffB);
;         PG8_WAIT_V(6); PG8_BAR;
.LBB0_981:
	v_readlane_b32 s0, v254, 38
	v_ashrrev_i32_e32 v7, 6, v6
	s_and_b32 s51, s0, 0x60
	v_and_b32_e32 v140, 15, v6
	v_ashrrev_i32_e32 v141, 4, v6
	v_and_b32_e32 v16, 48, v6
	v_lshlrev_b32_e32 v17, 10, v7
	v_lshlrev_b32_e32 v6, 2, v6
	s_lshr_b32 s0, s51, 3
	v_lshl_add_u64 v[8:9], s[44:45], 0, v[192:193]
	v_mov_b32_e32 v129, v193
	v_lshl_add_u32 v17, s12, 13, v17
	v_lshl_or_b32 v16, v140, 6, v16
	v_and_b32_e32 v6, 32, v6
	v_add_lshl_u32 v7, s0, v7, 10
	v_lshl_add_u64 v[10:11], s[44:45], 0, v[128:129]
	v_mov_b32_e32 v133, v193
	v_bitop3_b32 v17, v16, v17, v6 bitop3:0xde
	v_bitop3_b32 v142, v7, v16, v6 bitop3:0xf6
	s_add_i32 m0, s22, 0x18000
	v_lshl_add_u64 v[6:7], v[8:9], 0, s[28:29]
	v_lshl_add_u64 v[12:13], s[46:47], 0, v[132:133]
	v_mov_b32_e32 v131, v193
	s_lshl_b32 s50, s12, 6
	s_waitcnt vmcnt(2)
	s_barrier
	global_load_lds_dwordx4 v[6:7], off
	v_lshl_add_u64 v[6:7], v[10:11], 0, s[28:29]
	s_add_i32 m0, s22, 0x1a000
	s_add_i32 s52, s22, 0x8000
	s_add_i32 s53, s22, 0xa000
	v_lshl_add_u64 v[14:15], s[46:47], 0, v[130:131]
	global_load_lds_dwordx4 v[6:7], off
	v_lshl_add_u64 v[6:7], v[12:13], 0, s[28:29]
	s_mov_b32 m0, s52
	s_add_u32 s12, s44, 0x80080
	s_nop 0
	v_lshl_add_u64 v[6:7], v[14:15], 0, s[28:29]
	s_mov_b32 m0, s53
	s_addc_u32 s13, s45, 0
	s_nop 0
	s_add_i32 m0, s22, 0x1c000
	v_lshl_add_u64 v[6:7], s[12:13], 0, v[192:193]
	global_load_lds_dwordx4 v[6:7], off
	v_lshl_add_u64 v[6:7], s[12:13], 0, v[128:129]
	s_add_i32 m0, s22, 0x1e000
	s_cmp_lt_u32 s35, 4
	global_load_lds_dwordx4 v[6:7], off
	v_lshlrev_b32_e32 v6, 15, v0
	v_and_b32_e32 v6, 0xffff0000, v6
	v_lshl_add_u32 v1, v1, 12, v6
	v_and_b32_e32 v0, 1, v0
	v_lshl_or_b32 v0, v0, 6, v1
	v_lshl_add_u32 v134, v2, 1, v0
	v_lshlrev_b32_e32 v0, 15, v3
	v_and_b32_e32 v0, 0xffff0000, v0
	s_waitcnt vmcnt(4)
	v_lshl_add_u32 v0, v4, 12, v0
	v_and_b32_e32 v1, 1, v3
	v_lshl_or_b32 v0, v1, 6, v0
	v_readlane_b32 s0, v254, 20
	s_cselect_b64 s[12:13], -1, 0
	v_mov_b32_e32 v135, v193
	v_lshl_add_u32 v136, v5, 1, v0
	v_mov_b32_e32 v137, v193
	s_mov_b32 s54, 0
	v_add_u32_e32 v143, 0, v17
	v_readlane_b32 s55, v254, 9
	s_mov_b32 s56, s0
	s_barrier
	v_readlane_b32 s1, v254, 21
	s_branch .LBB0_984

; #define PG8_STAGE(bufoff, gbase, voff) do { _Pragma("unroll") for (int _i = 0; _i < 2; ++_i) \
;         __builtin_amdgcn_global_load_lds((const unsigned*)((const char*)(gbase) + (voff)[_i]), (PG8_LAS unsigned*)(lds + (bufoff) + ldsw + _i * 8192), 16, 0, 0); } while (0)
; #define PG8_LDA(dst, b, h) do { _Pragma("unroll") for (int m = 0; m < 4; ++m) _Pragma("unroll") for (int k = 0; k < 2; ++k) dst[m][k] = *(const PG8_LAS bf16x8*)(lds + PG8_SA(b, h) + aoff + m * 2048 + k * 1024); } while (0)
; #define PG8_LDB(dst, b, h) do { _Pragma("unroll") for (int n = 0; n < 2; ++n) _Pragma("unroll") for (int k = 0; k < 2; ++k) dst[n][k] = *(const PG8_LAS bf16x8*)(lds + PG8_SB(b, h) + boff + n * 2048 + k * 1024); } while (0)
; #define PG8_WAIT_V(n) asm volatile("s_waitcnt vmcnt(" #n ")" ::: "memory")
; #define PG8_WAIT_L(n) asm volatile("s_waitcnt lgkmcnt(" #n ")" ::: "memory")
; #define PG8_BAR __builtin_amdgcn_s_barrier()
; #define PG8_SCHED __builtin_amdgcn_sched_barrier(0)
; template <class Epi, class Sched, bool ALIGN_EPI = false, bool SP2 = false, bool F8 = false>
; __device__ __forceinline__ void gemm_phase(PG8_LAS unsigned char* lds, const Gemm g_in, const Sched& S, const Epi& E, int wave_in) {
;     ...
;             PG8_LDB(B0, 0, 0); PG8_LDB(B1, 0, 1); PG8_SCHED; PG8_LDA(At, 0, 0); PG8_STAGE(PG8_SA(1, 1), a1 + hstepA, voffA);
;             PG8_WAIT_V(8); PG8_WAIT_L(0); PG8_BAR; PG8_MMA(0, 0, At, B0); PG8_MMA(0, 1, At, B1); PG8_BAR; PG8_SCHED;
;             PG8_LDA(At, 0, 1); PG8_STAGE(PG8_SB(0, 0), b2, voffB); PG8_STAGE(PG8_SB(0, 1), b2 + hstepB, voffB); PG8_STAGE(PG8_SA(0, 0), a2, voffA);
;             PG8_WAIT_V(8); PG8_WAIT_L(0); PG8_BAR; PG8_MMA(1, 0, At, B0); PG8_MMA(1, 1, At, B1); PG8_BAR; PG8_SCHED;
.LBB0_991:
	s_add_u32 s0, s44, 0xfff80080
	s_addc_u32 s1, s45, -1
	s_cmp_eq_u32 s61, 28
	s_cselect_b32 s21, s17, s1
	s_cselect_b32 s20, s57, s0
	s_cselect_b32 s47, s15, s60
	s_cselect_b32 s46, s58, s59
	s_add_u32 s0, s44, 0xfff80000
	s_addc_u32 s1, s45, -1
	s_mov_b32 m0, s52
	s_nop 0
	global_load_lds_dwordx4 v132, s[0:1]
	s_mov_b32 m0, s53
	s_nop 0
	global_load_lds_dwordx4 v130, s[0:1]
	s_add_i32 m0, s22, 0xc000
	s_nop 0
	global_load_lds_dwordx4 v136, s[44:45]
	s_add_i32 m0, s22, 0xe000
	s_nop 0
	global_load_lds_dwordx4 v134, s[44:45]
	v_add_u32_e32 v138, 0x10000, v142
	ds_read_b128 v[144:147], v138
	ds_read_b128 v[148:151], v138 offset:1024
	ds_read_b128 v[152:155], v138 offset:2048
	ds_read_b128 v[156:159], v138 offset:3072
	v_add_u32_e32 v139, 0x14000, v142
	ds_read_b128 v[160:163], v139
	ds_read_b128 v[164:167], v139 offset:1024
	ds_read_b128 v[168:171], v139 offset:2048
	ds_read_b128 v[172:175], v139 offset:3072
	ds_read_b128 v[176:179], v143
	ds_read_b128 v[180:183], v143 offset:1024
	ds_read_b128 v[184:187], v143 offset:2048
	ds_read_b128 v[188:191], v143 offset:3072
	ds_read_b128 v[198:201], v143 offset:4096
	ds_read_b128 v[202:205], v143 offset:5120
	ds_read_b128 v[206:209], v143 offset:6144
	ds_read_b128 v[210:213], v143 offset:7168
	s_waitcnt vmcnt(8)
	s_waitcnt lgkmcnt(0)
	s_barrier
	s_setprio 1
	s_waitcnt lgkmcnt(0)
	v_mfma_f32_16x16x32_bf16 v[124:127], v[144:147], v[176:179], v[124:127]
	v_mfma_f32_16x16x32_bf16 v[120:123], v[152:155], v[176:179], v[120:123]
	v_mfma_f32_16x16x32_bf16 v[112:115], v[144:147], v[184:187], v[112:115]
	v_mfma_f32_16x16x32_bf16 v[104:107], v[152:155], v[184:187], v[104:107]
	v_mfma_f32_16x16x32_bf16 v[96:99], v[144:147], v[198:201], v[96:99]
	v_mfma_f32_16x16x32_bf16 v[88:91], v[152:155], v[198:201], v[88:91]
	v_mfma_f32_16x16x32_bf16 v[80:83], v[144:147], v[206:209], v[80:83]
	v_mfma_f32_16x16x32_bf16 v[72:75], v[152:155], v[206:209], v[72:75]
	v_mfma_f32_16x16x32_bf16 v[124:127], v[148:151], v[180:183], v[124:127]
	v_mfma_f32_16x16x32_bf16 v[120:123], v[156:159], v[180:183], v[120:123]
	v_mfma_f32_16x16x32_bf16 v[112:115], v[148:151], v[188:191], v[112:115]
	v_mfma_f32_16x16x32_bf16 v[104:107], v[156:159], v[188:191], v[104:107]
	v_mfma_f32_16x16x32_bf16 v[96:99], v[148:151], v[202:205], v[96:99]
	v_mfma_f32_16x16x32_bf16 v[88:91], v[156:159], v[202:205], v[88:91]
	v_mfma_f32_16x16x32_bf16 v[80:83], v[148:151], v[210:213], v[80:83]
	v_mfma_f32_16x16x32_bf16 v[72:75], v[156:159], v[210:213], v[72:75]
	s_setprio 0
	s_setprio 1
	v_mfma_f32_16x16x32_bf16 v[116:119], v[160:163], v[176:179], v[116:119]
	v_mfma_f32_16x16x32_bf16 v[108:111], v[168:171], v[176:179], v[108:111]
	v_mfma_f32_16x16x32_bf16 v[100:103], v[160:163], v[184:187], v[100:103]
	v_mfma_f32_16x16x32_bf16 v[92:95], v[168:171], v[184:187], v[92:95]
	v_mfma_f32_16x16x32_bf16 v[84:87], v[160:163], v[198:201], v[84:87]
	v_mfma_f32_16x16x32_bf16 v[76:79], v[168:171], v[198:201], v[76:79]
	v_mfma_f32_16x16x32_bf16 v[68:71], v[160:163], v[206:209], v[68:71]
	v_mfma_f32_16x16x32_bf16 v[64:67], v[168:171], v[206:209], v[64:67]
	v_mfma_f32_16x16x32_bf16 v[116:119], v[164:167], v[180:183], v[116:119]
	v_mfma_f32_16x16x32_bf16 v[108:111], v[172:175], v[180:183], v[108:111]
	v_mfma_f32_16x16x32_bf16 v[100:103], v[164:167], v[188:191], v[100:103]
	v_mfma_f32_16x16x32_bf16 v[92:95], v[172:175], v[188:191], v[92:95]
	v_mfma_f32_16x16x32_bf16 v[84:87], v[164:167], v[202:205], v[84:87]
	v_mfma_f32_16x16x32_bf16 v[76:79], v[172:175], v[202:205], v[76:79]
	v_mfma_f32_16x16x32_bf16 v[68:71], v[164:167], v[210:213], v[68:71]
	v_mfma_f32_16x16x32_bf16 v[64:67], v[172:175], v[210:213], v[64:67]
	s_setprio 0
	s_barrier
	s_add_u32 s62, s46, 0x80000
	s_addc_u32 s63, s47, 0
	s_add_i32 m0, s22, 0x10000
	s_nop 0
	global_load_lds_dwordx4 v192, s[46:47]
	s_add_i32 m0, s22, 0x12000
	s_nop 0
	global_load_lds_dwordx4 v128, s[46:47]
	s_add_i32 m0, s22, 0x14000
	s_nop 0
	global_load_lds_dwordx4 v192, s[62:63]
	s_add_i32 m0, s22, 0x16000
	s_nop 0
	global_load_lds_dwordx4 v128, s[62:63]
	ds_read_b128 v[176:179], v143 offset:16384
	ds_read_b128 v[180:183], v143 offset:17408
	ds_read_b128 v[184:187], v143 offset:18432
	ds_read_b128 v[188:191], v143 offset:19456
	ds_read_b128 v[198:201], v143 offset:20480
	ds_read_b128 v[202:205], v143 offset:21504
	ds_read_b128 v[206:209], v143 offset:22528
	ds_read_b128 v[210:213], v143 offset:23552
	s_waitcnt vmcnt(6)
	s_waitcnt lgkmcnt(0)
	s_barrier
	s_setprio 1
	s_waitcnt lgkmcnt(0)
	v_mfma_f32_16x16x32_bf16 v[60:63], v[144:147], v[176:179], v[60:63]
	v_mfma_f32_16x16x32_bf16 v[56:59], v[152:155], v[176:179], v[56:59]
	v_mfma_f32_16x16x32_bf16 v[48:51], v[144:147], v[184:187], v[48:51]
	v_mfma_f32_16x16x32_bf16 v[40:43], v[152:155], v[184:187], v[40:43]
	v_mfma_f32_16x16x32_bf16 v[32:35], v[144:147], v[198:201], v[32:35]
	v_mfma_f32_16x16x32_bf16 v[24:27], v[152:155], v[198:201], v[24:27]
	v_mfma_f32_16x16x32_bf16 v[16:19], v[144:147], v[206:209], v[16:19]
	v_mfma_f32_16x16x32_bf16 v[8:11], v[152:155], v[206:209], v[8:11]
	v_mfma_f32_16x16x32_bf16 v[60:63], v[148:151], v[180:183], v[60:63]
	v_mfma_f32_16x16x32_bf16 v[56:59], v[156:159], v[180:183], v[56:59]
	v_mfma_f32_16x16x32_bf16 v[48:51], v[148:151], v[188:191], v[48:51]
	v_mfma_f32_16x16x32_bf16 v[40:43], v[156:159], v[188:191], v[40:43]
	v_mfma_f32_16x16x32_bf16 v[32:35], v[148:151], v[202:205], v[32:35]
	v_mfma_f32_16x16x32_bf16 v[24:27], v[156:159], v[202:205], v[24:27]
	v_mfma_f32_16x16x32_bf16 v[16:19], v[148:151], v[210:213], v[16:19]
	v_mfma_f32_16x16x32_bf16 v[8:11], v[156:159], v[210:213], v[8:11]
	s_setprio 0
	s_setprio 1
	v_mfma_f32_16x16x32_bf16 v[52:55], v[160:163], v[176:179], v[52:55]
	v_mfma_f32_16x16x32_bf16 v[44:47], v[168:171], v[176:179], v[44:47]
	v_mfma_f32_16x16x32_bf16 v[36:39], v[160:163], v[184:187], v[36:39]
	v_mfma_f32_16x16x32_bf16 v[28:31], v[168:171], v[184:187], v[28:31]
	v_mfma_f32_16x16x32_bf16 v[20:23], v[160:163], v[198:201], v[20:23]
	v_mfma_f32_16x16x32_bf16 v[12:15], v[168:171], v[198:201], v[12:15]
	v_mfma_f32_16x16x32_bf16 v[4:7], v[160:163], v[206:209], v[4:7]
	v_mfma_f32_16x16x32_bf16 v[0:3], v[168:171], v[206:209], v[0:3]
	v_mfma_f32_16x16x32_bf16 v[52:55], v[164:167], v[180:183], v[52:55]
	v_mfma_f32_16x16x32_bf16 v[44:47], v[172:175], v[180:183], v[44:47]
	v_mfma_f32_16x16x32_bf16 v[36:39], v[164:167], v[188:191], v[36:39]
	v_mfma_f32_16x16x32_bf16 v[28:31], v[172:175], v[188:191], v[28:31]
	v_mfma_f32_16x16x32_bf16 v[20:23], v[164:167], v[202:205], v[20:23]
	v_mfma_f32_16x16x32_bf16 v[12:15], v[172:175], v[202:205], v[12:15]
	v_mfma_f32_16x16x32_bf16 v[4:7], v[164:167], v[210:213], v[4:7]
	v_mfma_f32_16x16x32_bf16 v[0:3], v[172:175], v[210:213], v[0:3]
	s_setprio 0
	s_barrier
; #define PG8_STAGE(bufoff, gbase, voff) do { _Pragma("unroll") for (int _i = 0; _i < 2; ++_i) \
;         __builtin_amdgcn_global_load_lds((const unsigned*)((const char*)(gbase) + (voff)[_i]), (PG8_LAS unsigned*)(lds + (bufoff) + ldsw + _i * 8192), 16, 0, 0); } while (0)
; #define PG8_LDA(dst, b, h) do { _Pragma("unroll") for (int m = 0; m < 4; ++m) _Pragma("unroll") for (int k = 0; k < 2; ++k) dst[m][k] = *(const PG8_LAS bf16x8*)(lds + PG8_SA(b, h) + aoff + m * 2048 + k * 1024); } while (0)
; #define PG8_LDB(dst, b, h) do { _Pragma("unroll") for (int n = 0; n < 2; ++n) _Pragma("unroll") for (int k = 0; k < 2; ++k) dst[n][k] = *(const PG8_LAS bf16x8*)(lds + PG8_SB(b, h) + boff + n * 2048 + k * 1024); } while (0)
; #define PG8_WAIT_V(n) asm volatile("s_waitcnt vmcnt(" #n ")" ::: "memory")
; #define PG8_WAIT_L(n) asm volatile("s_waitcnt lgkmcnt(" #n ")" ::: "memory")
; #define PG8_BAR __builtin_amdgcn_s_barrier()
; #define PG8_SCHED __builtin_amdgcn_sched_barrier(0)
; template <class Epi, class Sched, bool ALIGN_EPI = false, bool SP2 = false, bool F8 = false>
; __device__ __forceinline__ void gemm_phase(PG8_LAS unsigned char* lds, const Gemm g_in, const Sched& S, const Epi& E, int wave_in) {
;     ...
;             PG8_LDB(B0, 1, 0); PG8_LDB(B1, 1, 1); PG8_SCHED; PG8_LDA(At, 1, 0); PG8_STAGE(PG8_SA(0, 1), a2 + hstepA, voffA);
;             PG8_WAIT_V(8); PG8_WAIT_L(0); PG8_BAR; PG8_MMA(0, 0, At, B0); PG8_MMA(0, 1, At, B1); PG8_BAR; PG8_SCHED;
;             PG8_LDA(At, 1, 1); PG8_STAGE(PG8_SB(1, 0), b3, voffB); PG8_STAGE(PG8_SB(1, 1), b3 + hstepB, voffB); PG8_STAGE(PG8_SA(1, 0), a3, voffA);
;             PG8_WAIT_V(8); PG8_WAIT_L(0); PG8_BAR; PG8_MMA(1, 0, At, B0); PG8_MMA(1, 1, At, B1); PG8_BAR; PG8_SCHED;
	s_add_u32 s0, s20, 0x80000
	s_addc_u32 s1, s21, 0
	s_mov_b32 m0, s22
	s_nop 0
	global_load_lds_dwordx4 v132, s[20:21]
	s_mov_b32 m0, s23
	s_nop 0
	global_load_lds_dwordx4 v130, s[20:21]
	s_mov_b32 m0, s48
	s_nop 0
	global_load_lds_dwordx4 v132, s[0:1]
	s_mov_b32 m0, s49
	s_nop 0
	global_load_lds_dwordx4 v130, s[0:1]
	v_add_u32_e32 v138, 0x18000, v142
	ds_read_b128 v[144:147], v138
	ds_read_b128 v[148:151], v138 offset:1024
	ds_read_b128 v[152:155], v138 offset:2048
	ds_read_b128 v[156:159], v138 offset:3072
	v_add_u32_e32 v139, 0x1c000, v142
	ds_read_b128 v[160:163], v139
	ds_read_b128 v[164:167], v139 offset:1024
	ds_read_b128 v[168:171], v139 offset:2048
	ds_read_b128 v[172:175], v139 offset:3072
	ds_read_b128 v[176:179], v143 offset:32768
	ds_read_b128 v[180:183], v143 offset:33792
	ds_read_b128 v[184:187], v143 offset:34816
	ds_read_b128 v[188:191], v143 offset:35840
	ds_read_b128 v[198:201], v143 offset:36864
	ds_read_b128 v[202:205], v143 offset:37888
	ds_read_b128 v[206:209], v143 offset:38912
	ds_read_b128 v[210:213], v143 offset:39936
	s_waitcnt vmcnt(8)
	s_waitcnt lgkmcnt(0)
	s_barrier
	s_setprio 1
	s_waitcnt lgkmcnt(0)
	v_mfma_f32_16x16x32_bf16 v[124:127], v[144:147], v[176:179], v[124:127]
	v_mfma_f32_16x16x32_bf16 v[120:123], v[152:155], v[176:179], v[120:123]
	v_mfma_f32_16x16x32_bf16 v[112:115], v[144:147], v[184:187], v[112:115]
	v_mfma_f32_16x16x32_bf16 v[104:107], v[152:155], v[184:187], v[104:107]
	v_mfma_f32_16x16x32_bf16 v[96:99], v[144:147], v[198:201], v[96:99]
	v_mfma_f32_16x16x32_bf16 v[88:91], v[152:155], v[198:201], v[88:91]
	v_mfma_f32_16x16x32_bf16 v[80:83], v[144:147], v[206:209], v[80:83]
	v_mfma_f32_16x16x32_bf16 v[72:75], v[152:155], v[206:209], v[72:75]
	v_mfma_f32_16x16x32_bf16 v[124:127], v[148:151], v[180:183], v[124:127]
	v_mfma_f32_16x16x32_bf16 v[120:123], v[156:159], v[180:183], v[120:123]
	v_mfma_f32_16x16x32_bf16 v[112:115], v[148:151], v[188:191], v[112:115]
	v_mfma_f32_16x16x32_bf16 v[104:107], v[156:159], v[188:191], v[104:107]
	v_mfma_f32_16x16x32_bf16 v[96:99], v[148:151], v[202:205], v[96:99]
	v_mfma_f32_16x16x32_bf16 v[88:91], v[156:159], v[202:205], v[88:91]
	v_mfma_f32_16x16x32_bf16 v[80:83], v[148:151], v[210:213], v[80:83]
	v_mfma_f32_16x16x32_bf16 v[72:75], v[156:159], v[210:213], v[72:75]
	s_setprio 0
	s_setprio 1
	v_mfma_f32_16x16x32_bf16 v[116:119], v[160:163], v[176:179], v[116:119]
	v_mfma_f32_16x16x32_bf16 v[108:111], v[168:171], v[176:179], v[108:111]
	v_mfma_f32_16x16x32_bf16 v[100:103], v[160:163], v[184:187], v[100:103]
	v_mfma_f32_16x16x32_bf16 v[92:95], v[168:171], v[184:187], v[92:95]
	v_mfma_f32_16x16x32_bf16 v[84:87], v[160:163], v[198:201], v[84:87]
	v_mfma_f32_16x16x32_bf16 v[76:79], v[168:171], v[198:201], v[76:79]
	v_mfma_f32_16x16x32_bf16 v[68:71], v[160:163], v[206:209], v[68:71]
	v_mfma_f32_16x16x32_bf16 v[64:67], v[168:171], v[206:209], v[64:67]
	v_mfma_f32_16x16x32_bf16 v[116:119], v[164:167], v[180:183], v[116:119]
	v_mfma_f32_16x16x32_bf16 v[108:111], v[172:175], v[180:183], v[108:111]
	v_mfma_f32_16x16x32_bf16 v[100:103], v[164:167], v[188:191], v[100:103]
	v_mfma_f32_16x16x32_bf16 v[92:95], v[172:175], v[188:191], v[92:95]
	v_mfma_f32_16x16x32_bf16 v[84:87], v[164:167], v[202:205], v[84:87]
	v_mfma_f32_16x16x32_bf16 v[76:79], v[172:175], v[202:205], v[76:79]
	v_mfma_f32_16x16x32_bf16 v[68:71], v[164:167], v[210:213], v[68:71]
	v_mfma_f32_16x16x32_bf16 v[64:67], v[172:175], v[210:213], v[64:67]
	s_setprio 0
	s_barrier
	s_add_u32 s62, s46, 0x80
	s_addc_u32 s63, s47, 0
	s_add_u32 s0, s46, 0x80080
	s_addc_u32 s1, s47, 0
	s_add_i32 m0, s22, 0x18000
	s_nop 0
	global_load_lds_dwordx4 v192, s[62:63]
	s_add_i32 m0, s22, 0x1a000
	s_nop 0
	global_load_lds_dwordx4 v128, s[62:63]
	s_add_i32 m0, s22, 0x1c000
	s_nop 0
	global_load_lds_dwordx4 v192, s[0:1]
	s_add_i32 m0, s22, 0x1e000
	s_nop 0
	global_load_lds_dwordx4 v128, s[0:1]
	ds_read_b128 v[176:179], v143 offset:49152
	ds_read_b128 v[180:183], v143 offset:50176
	ds_read_b128 v[184:187], v143 offset:51200
	ds_read_b128 v[188:191], v143 offset:52224
	ds_read_b128 v[198:201], v143 offset:53248
	ds_read_b128 v[202:205], v143 offset:54272
	ds_read_b128 v[206:209], v143 offset:55296
	ds_read_b128 v[210:213], v143 offset:56320
	s_waitcnt vmcnt(6)
	s_waitcnt lgkmcnt(0)
	s_barrier
	s_setprio 1
	s_waitcnt lgkmcnt(0)
	v_mfma_f32_16x16x32_bf16 v[60:63], v[144:147], v[176:179], v[60:63]
	v_mfma_f32_16x16x32_bf16 v[56:59], v[152:155], v[176:179], v[56:59]
	v_mfma_f32_16x16x32_bf16 v[48:51], v[144:147], v[184:187], v[48:51]
	v_mfma_f32_16x16x32_bf16 v[40:43], v[152:155], v[184:187], v[40:43]
	v_mfma_f32_16x16x32_bf16 v[32:35], v[144:147], v[198:201], v[32:35]
	v_mfma_f32_16x16x32_bf16 v[24:27], v[152:155], v[198:201], v[24:27]
	v_mfma_f32_16x16x32_bf16 v[16:19], v[144:147], v[206:209], v[16:19]
	v_mfma_f32_16x16x32_bf16 v[8:11], v[152:155], v[206:209], v[8:11]
	v_mfma_f32_16x16x32_bf16 v[60:63], v[148:151], v[180:183], v[60:63]
	v_mfma_f32_16x16x32_bf16 v[56:59], v[156:159], v[180:183], v[56:59]
	v_mfma_f32_16x16x32_bf16 v[48:51], v[148:151], v[188:191], v[48:51]
	v_mfma_f32_16x16x32_bf16 v[40:43], v[156:159], v[188:191], v[40:43]
	v_mfma_f32_16x16x32_bf16 v[32:35], v[148:151], v[202:205], v[32:35]
	v_mfma_f32_16x16x32_bf16 v[24:27], v[156:159], v[202:205], v[24:27]
	v_mfma_f32_16x16x32_bf16 v[16:19], v[148:151], v[210:213], v[16:19]
	v_mfma_f32_16x16x32_bf16 v[8:11], v[156:159], v[210:213], v[8:11]
	s_setprio 0
	s_setprio 1
	v_mfma_f32_16x16x32_bf16 v[52:55], v[160:163], v[176:179], v[52:55]
	v_mfma_f32_16x16x32_bf16 v[44:47], v[168:171], v[176:179], v[44:47]
	v_mfma_f32_16x16x32_bf16 v[36:39], v[160:163], v[184:187], v[36:39]
	v_mfma_f32_16x16x32_bf16 v[28:31], v[168:171], v[184:187], v[28:31]
	v_mfma_f32_16x16x32_bf16 v[20:23], v[160:163], v[198:201], v[20:23]
	v_mfma_f32_16x16x32_bf16 v[12:15], v[168:171], v[198:201], v[12:15]
	v_mfma_f32_16x16x32_bf16 v[4:7], v[160:163], v[206:209], v[4:7]
	v_mfma_f32_16x16x32_bf16 v[0:3], v[168:171], v[206:209], v[0:3]
	v_mfma_f32_16x16x32_bf16 v[52:55], v[164:167], v[180:183], v[52:55]
	v_mfma_f32_16x16x32_bf16 v[44:47], v[172:175], v[180:183], v[44:47]
	v_mfma_f32_16x16x32_bf16 v[36:39], v[164:167], v[188:191], v[36:39]
	v_mfma_f32_16x16x32_bf16 v[28:31], v[172:175], v[188:191], v[28:31]
	v_mfma_f32_16x16x32_bf16 v[20:23], v[164:167], v[202:205], v[20:23]
	v_mfma_f32_16x16x32_bf16 v[12:15], v[172:175], v[202:205], v[12:15]
	v_mfma_f32_16x16x32_bf16 v[4:7], v[164:167], v[210:213], v[4:7]
	v_mfma_f32_16x16x32_bf16 v[0:3], v[172:175], v[210:213], v[0:3]
	s_setprio 0
	s_barrier
	s_add_i32 s61, s61, 2
	s_add_u32 s59, s59, 0x100
	s_addc_u32 s60, s60, 0
	s_add_u32 s44, s44, 0x100
	s_addc_u32 s45, s45, 0
	s_cmp_gt_u32 s61, 29
	s_cbranch_scc0 .LBB0_991
	s_and_b64 vcc, exec, s[12:13]
	s_cbranch_vccz .LBB0_994
	s_barrier
